# P9 down-projection epilogue: b_down slices prefetched at unit-loop top (no exposed bias-load wait)
# baseline (speedup 1.0000x reference)
.LBB0_1320:
	v_lshl_or_b32 v232, s0, 8, v168
	v_ashrrev_i32_e32 v233, 31, v232
	v_lshl_add_u64 v[232:233], v[232:233], 2, s[10:11]
	global_load_dwordx4 v[216:219], v[232:233], off
	global_load_dwordx4 v[206:209], v[232:233], off offset:16
	global_load_dwordx4 v[228:231], v[232:233], off offset:512
	global_load_dwordx4 v[224:227], v[232:233], off offset:528
	s_add_i32 s59, s59, 1
	v_readlane_b32 s1, v252, 17
	s_mul_i32 s19, s59, s1
	v_readlane_b32 s1, v252, 19
	s_add_i32 s19, s19, s1
	s_ashr_i32 s1, s19, 31
	s_lshr_b32 s1, s1, 30
	s_add_i32 s1, s19, s1
	s_ashr_i32 s21, s1, 2
	s_lshl_b32 s1, s21, 3
	v_readlane_b32 s22, v252, 18
	s_or_b32 s1, s1, s22
	s_cmp_lt_i32 s1, s33
	s_cselect_b64 s[26:27], -1, 0
	s_cmp_ge_i32 s1, s33
	s_cbranch_scc1 .LBB0_1322
	s_lshl_b32 s18, s21, 2
	s_sub_i32 s18, s19, s18
	s_lshl_b32 s19, s1, 1
	s_add_i32 s19, s19, 0
	s_add_i32 s19, s19, 0x201e0
	v_mov_b32_e32 v2, s19
	ds_read_u16 v2, v2
	s_mov_b32 s20, s1
	s_waitcnt lgkmcnt(0)
	v_readfirstlane_b32 s19, v2
	s_and_b32 s19, s19, 0xffff
	s_lshl_b32 s19, s19, 2
	s_add_i32 s18, s18, s19

.LBB0_1326:
	v_lshl_or_b32 v18, s0, 8, v168
	v_ashrrev_i32_e32 v19, 31, v18
	s_mov_b32 s64, 0x1f000
	s_nop 15
	s_nop 3
.LBB0_1328:
.LBB0_1330:
	s_movk_i32 s66, 0x1800
.LBB0_1332:
.LBB0_1334:
	v_lshrrev_b32_e32 v19, 22, v19
	v_add_u32_e32 v19, v18, v19
	v_lshl_add_u32 v24, s60, 8, v167
	v_and_b32_e32 v19, 0xfffffc00, v19
	v_sub_u32_e32 v18, v18, v19
	v_ashrrev_i32_e32 v25, 31, v24
	v_ashrrev_i32_e32 v19, 31, v18
	v_lshlrev_b64 v[20:21], 11, v[24:25]
	v_lshl_add_u64 v[20:21], s[8:9], 0, v[20:21]
	v_lshlrev_b64 v[26:27], 1, v[18:19]
	v_lshl_add_u64 v[18:19], v[20:21], 0, v[26:27]
	v_pk_add_f32 v[22:23], v[152:153], v[218:219]
	v_pk_add_f32 v[20:21], v[150:151], v[216:217]
	v_pk_add_f32 v[28:29], v[148:149], v[208:209]
	v_pk_add_f32 v[30:31], v[146:147], v[206:207]
	v_cvt_pk_bf16_f32 v20, v20, v21
	v_cvt_pk_bf16_f32 v21, v22, v23
	v_cvt_pk_bf16_f32 v22, v30, v31
	v_cvt_pk_bf16_f32 v23, v28, v29
	global_store_dwordx4 v[18:19], v[20:23], off
	v_pk_add_f32 v[28:29], v[156:157], v[226:227]
	v_pk_add_f32 v[30:31], v[154:155], v[224:225]
	v_pk_add_f32 v[22:23], v[160:161], v[230:231]
	v_pk_add_f32 v[20:21], v[158:159], v[228:229]
	v_pk_add_f32 v[32:33], v[134:135], v[206:207]
	v_cvt_pk_bf16_f32 v20, v20, v21
	v_cvt_pk_bf16_f32 v21, v22, v23
	v_cvt_pk_bf16_f32 v22, v30, v31
	v_cvt_pk_bf16_f32 v23, v28, v29
	global_store_dwordx4 v[18:19], v[20:23], off offset:256
	v_pk_add_f32 v[30:31], v[136:137], v[208:209]
	s_mov_b64 s[0:1], 0x40000
	v_or_b32_e32 v20, 16, v24
	v_ashrrev_i32_e32 v21, 31, v20
	v_lshlrev_b64 v[20:21], 11, v[20:21]
	v_lshl_add_u64 v[20:21], s[8:9], 0, v[20:21]
	v_lshl_add_u64 v[28:29], v[20:21], 0, v[26:27]
	v_pk_add_f32 v[22:23], v[132:133], v[218:219]
	v_pk_add_f32 v[20:21], v[130:131], v[216:217]
	s_nop 0
	v_cvt_pk_bf16_f32 v20, v20, v21
	v_cvt_pk_bf16_f32 v21, v22, v23
	v_cvt_pk_bf16_f32 v22, v32, v33
	v_cvt_pk_bf16_f32 v23, v30, v31
	global_store_dwordx4 v[28:29], v[20:23], off
	v_pk_add_f32 v[30:31], v[144:145], v[226:227]
	v_pk_add_f32 v[32:33], v[142:143], v[224:225]
	v_pk_add_f32 v[22:23], v[140:141], v[230:231]
	v_pk_add_f32 v[20:21], v[138:139], v[228:229]
	s_nop 0
	v_cvt_pk_bf16_f32 v20, v20, v21
	v_cvt_pk_bf16_f32 v21, v22, v23
	v_cvt_pk_bf16_f32 v22, v32, v33
	v_cvt_pk_bf16_f32 v23, v30, v31
	global_store_dwordx4 v[28:29], v[20:23], off offset:256
	v_pk_add_f32 v[30:31], v[112:113], v[208:209]
	v_pk_add_f32 v[32:33], v[110:111], v[206:207]
	v_or_b32_e32 v20, 32, v24
	v_ashrrev_i32_e32 v21, 31, v20
	v_lshlrev_b64 v[20:21], 11, v[20:21]
	v_lshl_add_u64 v[20:21], s[8:9], 0, v[20:21]
	v_lshl_add_u64 v[28:29], v[20:21], 0, v[26:27]
	v_pk_add_f32 v[22:23], v[108:109], v[218:219]
	v_pk_add_f32 v[20:21], v[106:107], v[216:217]
	s_nop 0
	v_cvt_pk_bf16_f32 v20, v20, v21
	v_cvt_pk_bf16_f32 v21, v22, v23
	v_cvt_pk_bf16_f32 v22, v32, v33
	v_cvt_pk_bf16_f32 v23, v30, v31
	global_store_dwordx4 v[28:29], v[20:23], off
	v_pk_add_f32 v[30:31], v[128:129], v[226:227]
	v_pk_add_f32 v[32:33], v[126:127], v[224:225]
	v_pk_add_f32 v[22:23], v[124:125], v[230:231]
	v_pk_add_f32 v[20:21], v[122:123], v[228:229]
	s_nop 0
	v_cvt_pk_bf16_f32 v20, v20, v21
	v_cvt_pk_bf16_f32 v21, v22, v23
	v_cvt_pk_bf16_f32 v22, v32, v33
	v_cvt_pk_bf16_f32 v23, v30, v31
	global_store_dwordx4 v[28:29], v[20:23], off offset:256
	v_pk_add_f32 v[28:29], v[78:79], v[206:207]
	s_nop 0
	v_or_b32_e32 v20, 48, v24
	v_ashrrev_i32_e32 v21, 31, v20
	v_lshlrev_b64 v[20:21], 11, v[20:21]
	v_lshl_add_u64 v[20:21], s[8:9], 0, v[20:21]
	v_lshl_add_u64 v[24:25], v[20:21], 0, v[26:27]
	v_pk_add_f32 v[22:23], v[76:77], v[218:219]
	v_pk_add_f32 v[20:21], v[74:75], v[216:217]
	v_pk_add_f32 v[26:27], v[80:81], v[208:209]
	v_cvt_pk_bf16_f32 v20, v20, v21
	v_cvt_pk_bf16_f32 v21, v22, v23
	v_cvt_pk_bf16_f32 v22, v28, v29
	v_cvt_pk_bf16_f32 v23, v26, v27
	global_store_dwordx4 v[24:25], v[20:23], off
	v_pk_add_f32 v[26:27], v[104:105], v[226:227]
	v_pk_add_f32 v[28:29], v[102:103], v[224:225]
	v_pk_add_f32 v[22:23], v[100:101], v[230:231]
	v_pk_add_f32 v[20:21], v[98:99], v[228:229]
	s_nop 0
	v_cvt_pk_bf16_f32 v20, v20, v21
	v_cvt_pk_bf16_f32 v21, v22, v23
	v_cvt_pk_bf16_f32 v22, v28, v29
	v_cvt_pk_bf16_f32 v23, v26, v27
	global_store_dwordx4 v[24:25], v[20:23], off offset:256
	v_lshl_add_u64 v[24:25], v[18:19], 0, s[0:1]
	v_pk_add_f32 v[26:27], v[96:97], v[208:209]
	v_pk_add_f32 v[22:23], v[92:93], v[218:219]
	v_pk_add_f32 v[20:21], v[90:91], v[216:217]
	s_mov_b32 s0, 0x40000
	v_pk_add_f32 v[28:29], v[94:95], v[206:207]
	v_cvt_pk_bf16_f32 v20, v20, v21
	v_cvt_pk_bf16_f32 v21, v22, v23
	v_cvt_pk_bf16_f32 v23, v26, v27
	v_add_co_u32_e32 v26, vcc, s0, v18
	v_cvt_pk_bf16_f32 v22, v28, v29
	s_nop 0
	v_addc_co_u32_e32 v27, vcc, 0, v19, vcc
	global_store_dwordx4 v[26:27], v[20:23], off
	v_pk_add_f32 v[26:27], v[120:121], v[226:227]
	v_pk_add_f32 v[28:29], v[118:119], v[224:225]
	v_pk_add_f32 v[22:23], v[116:117], v[230:231]
	v_pk_add_f32 v[20:21], v[114:115], v[228:229]
	s_mov_b64 s[0:1], 0x48000
	v_cvt_pk_bf16_f32 v20, v20, v21
	v_cvt_pk_bf16_f32 v21, v22, v23
	v_cvt_pk_bf16_f32 v22, v28, v29
	v_cvt_pk_bf16_f32 v23, v26, v27
	global_store_dwordx4 v[24:25], v[20:23], off offset:256
	v_lshl_add_u64 v[24:25], v[18:19], 0, s[0:1]
	v_pk_add_f32 v[26:27], v[72:73], v[208:209]
	v_pk_add_f32 v[22:23], v[68:69], v[218:219]
	v_pk_add_f32 v[20:21], v[66:67], v[216:217]
	s_mov_b32 s0, 0x48000
	v_pk_add_f32 v[28:29], v[70:71], v[206:207]
	v_cvt_pk_bf16_f32 v20, v20, v21
	v_cvt_pk_bf16_f32 v21, v22, v23
	v_cvt_pk_bf16_f32 v23, v26, v27
	v_add_co_u32_e32 v26, vcc, s0, v18
	v_cvt_pk_bf16_f32 v22, v28, v29
	s_nop 0
	v_addc_co_u32_e32 v27, vcc, 0, v19, vcc
	global_store_dwordx4 v[26:27], v[20:23], off
	v_pk_add_f32 v[26:27], v[88:89], v[226:227]
	v_pk_add_f32 v[28:29], v[86:87], v[224:225]
	v_pk_add_f32 v[22:23], v[84:85], v[230:231]
	v_pk_add_f32 v[20:21], v[82:83], v[228:229]
	s_mov_b64 s[0:1], 0x50000
	v_cvt_pk_bf16_f32 v20, v20, v21
	v_cvt_pk_bf16_f32 v21, v22, v23
	v_cvt_pk_bf16_f32 v22, v28, v29
	v_cvt_pk_bf16_f32 v23, v26, v27
	global_store_dwordx4 v[24:25], v[20:23], off offset:256
	v_lshl_add_u64 v[24:25], v[18:19], 0, s[0:1]
	v_pk_add_f32 v[26:27], v[56:57], v[208:209]
	v_pk_add_f32 v[22:23], v[52:53], v[218:219]
	v_pk_add_f32 v[20:21], v[50:51], v[216:217]
	s_mov_b32 s0, 0x50000
	v_pk_add_f32 v[28:29], v[54:55], v[206:207]
	v_cvt_pk_bf16_f32 v20, v20, v21
	v_cvt_pk_bf16_f32 v21, v22, v23
	v_cvt_pk_bf16_f32 v23, v26, v27
	v_add_co_u32_e32 v26, vcc, s0, v18
	v_cvt_pk_bf16_f32 v22, v28, v29
	s_nop 0
	v_addc_co_u32_e32 v27, vcc, 0, v19, vcc
	global_store_dwordx4 v[26:27], v[20:23], off
	v_pk_add_f32 v[26:27], v[64:65], v[226:227]
	v_pk_add_f32 v[28:29], v[62:63], v[224:225]
	v_pk_add_f32 v[22:23], v[60:61], v[230:231]
	v_pk_add_f32 v[20:21], v[58:59], v[228:229]
	s_mov_b64 s[0:1], 0x58000
	v_cvt_pk_bf16_f32 v20, v20, v21
	v_cvt_pk_bf16_f32 v21, v22, v23
	v_cvt_pk_bf16_f32 v22, v28, v29
	v_cvt_pk_bf16_f32 v23, v26, v27
	global_store_dwordx4 v[24:25], v[20:23], off offset:256
	v_pk_add_f32 v[216:217], v[38:39], v[216:217]
	v_pk_add_f32 v[218:219], v[40:41], v[218:219]
	v_lshl_add_u64 v[20:21], v[18:19], 0, s[0:1]
	s_mov_b32 s0, 0x58000
	v_pk_add_f32 v[22:23], v[44:45], v[208:209]
	v_pk_add_f32 v[208:209], v[42:43], v[206:207]
	v_cvt_pk_bf16_f32 v206, v216, v217
	v_add_co_u32_e32 v216, vcc, s0, v18
	v_cvt_pk_bf16_f32 v207, v218, v219
	v_cvt_pk_bf16_f32 v208, v208, v209
	v_cvt_pk_bf16_f32 v209, v22, v23
	v_addc_co_u32_e32 v217, vcc, 0, v19, vcc
	global_store_dwordx4 v[216:217], v[206:209], off
	v_pk_add_f32 v[216:217], v[36:37], v[226:227]
	v_pk_add_f32 v[218:219], v[34:35], v[224:225]
	v_pk_add_f32 v[208:209], v[48:49], v[230:231]
	v_pk_add_f32 v[206:207], v[46:47], v[228:229]
	s_andn2_b64 vcc, exec, s[26:27]
	v_cvt_pk_bf16_f32 v206, v206, v207
	v_cvt_pk_bf16_f32 v207, v208, v209
	v_cvt_pk_bf16_f32 v208, v218, v219
	v_cvt_pk_bf16_f32 v209, v216, v217
	s_mov_b64 s[0:1], -1
	global_store_dwordx4 v[20:21], v[206:209], off offset:256
	s_cbranch_vccnz .LBB0_1319
	v_readlane_b32 s28, v253, 4
	v_readlane_b32 s30, v253, 6
	v_readlane_b32 s31, v253, 7
	v_readlane_b32 s29, v253, 5
	s_and_b64 vcc, exec, s[4:5]
	v_mov_b64_e32 v[36:37], s[30:31]
	v_mov_b64_e32 v[152:153], s[30:31]
	v_mov_b64_e32 v[148:149], s[30:31]
	v_mov_b64_e32 v[132:133], s[30:31]
	v_mov_b64_e32 v[136:137], s[30:31]
	v_mov_b64_e32 v[108:109], s[30:31]
	v_mov_b64_e32 v[112:113], s[30:31]
	v_mov_b64_e32 v[76:77], s[30:31]
	v_mov_b64_e32 v[80:81], s[30:31]
	v_mov_b64_e32 v[160:161], s[30:31]
	v_mov_b64_e32 v[156:157], s[30:31]
	v_mov_b64_e32 v[140:141], s[30:31]
	v_mov_b64_e32 v[144:145], s[30:31]
	v_mov_b64_e32 v[124:125], s[30:31]
	v_mov_b64_e32 v[128:129], s[30:31]
	v_mov_b64_e32 v[100:101], s[30:31]
	v_mov_b64_e32 v[104:105], s[30:31]
	v_mov_b64_e32 v[92:93], s[30:31]
	v_mov_b64_e32 v[96:97], s[30:31]
	v_mov_b64_e32 v[68:69], s[30:31]
	v_mov_b64_e32 v[72:73], s[30:31]
	v_mov_b64_e32 v[52:53], s[30:31]
	v_mov_b64_e32 v[56:57], s[30:31]
	v_mov_b64_e32 v[40:41], s[30:31]
	v_mov_b64_e32 v[44:45], s[30:31]
	v_mov_b64_e32 v[116:117], s[30:31]
	v_mov_b64_e32 v[120:121], s[30:31]
	v_mov_b64_e32 v[84:85], s[30:31]
	v_mov_b64_e32 v[88:89], s[30:31]
	v_mov_b64_e32 v[60:61], s[30:31]
	v_mov_b64_e32 v[64:65], s[30:31]
	v_mov_b64_e32 v[48:49], s[30:31]
	v_mov_b64_e32 v[34:35], s[28:29]
	v_mov_b64_e32 v[150:151], s[28:29]
	v_mov_b64_e32 v[146:147], s[28:29]
	v_mov_b64_e32 v[130:131], s[28:29]
	v_mov_b64_e32 v[134:135], s[28:29]
	v_mov_b64_e32 v[106:107], s[28:29]
	v_mov_b64_e32 v[110:111], s[28:29]
	v_mov_b64_e32 v[74:75], s[28:29]
	v_mov_b64_e32 v[78:79], s[28:29]
	v_mov_b64_e32 v[158:159], s[28:29]
	v_mov_b64_e32 v[154:155], s[28:29]
	v_mov_b64_e32 v[138:139], s[28:29]
	v_mov_b64_e32 v[142:143], s[28:29]
	v_mov_b64_e32 v[122:123], s[28:29]
	v_mov_b64_e32 v[126:127], s[28:29]
	v_mov_b64_e32 v[98:99], s[28:29]
	v_mov_b64_e32 v[102:103], s[28:29]
	v_mov_b64_e32 v[90:91], s[28:29]
	v_mov_b64_e32 v[94:95], s[28:29]
	v_mov_b64_e32 v[66:67], s[28:29]
	v_mov_b64_e32 v[70:71], s[28:29]
	v_mov_b64_e32 v[50:51], s[28:29]
	v_mov_b64_e32 v[54:55], s[28:29]
	v_mov_b64_e32 v[38:39], s[28:29]
	v_mov_b64_e32 v[42:43], s[28:29]
	v_mov_b64_e32 v[114:115], s[28:29]
	v_mov_b64_e32 v[118:119], s[28:29]
	v_mov_b64_e32 v[82:83], s[28:29]
	v_mov_b64_e32 v[86:87], s[28:29]
	v_mov_b64_e32 v[58:59], s[28:29]
	v_mov_b64_e32 v[62:63], s[28:29]
	v_mov_b64_e32 v[46:47], s[28:29]
	s_cbranch_vccz .LBB0_1318
	s_barrier
	s_branch .LBB0_1318
